# y stores write-through again except the pass-1 store that covers the pointer-slot line (plain, so stale copies of that line get invalidated)
# speedup vs baseline: 1.4696x; 1.0010x over previous
.LBB3_74:
	s_waitcnt lgkmcnt(0)
	s_barrier
	s_lshl_b32 s0, s33, 19
	v_add_u32_e32 v14, s96, v16
	v_lshlrev_b32_e32 v0, 4, v16
	s_add_u32 s0, s66, s0
	v_and_b32_e32 v0, 0xf0, v0
	v_ashrrev_i32_e32 v4, 4, v14
	s_addc_u32 s1, s67, 0
	v_add_u32_e32 v15, s78, v0
	v_mov_b32_e32 v1, 0
	v_ashrrev_i32_e32 v5, 31, v4
	v_lshl_add_u64 v[8:9], s[0:1], 0, v[0:1]
	v_lshl_add_u32 v0, v4, 8, v15
	v_lshlrev_b64 v[4:5], 12, v[4:5]
	v_lshl_add_u64 v[10:11], v[8:9], 0, v[4:5]
	v_add_u32_e32 v4, 0x200, v14
	ds_read_b128 v[0:3], v0
	v_ashrrev_i32_e32 v12, 4, v4
	v_lshl_add_u32 v4, v12, 8, v15
	ds_read_b128 v[4:7], v4
	v_ashrrev_i32_e32 v13, 31, v12
	s_waitcnt lgkmcnt(1)
	global_store_dwordx4 v[10:11], v[0:3], off
	s_nop 1
	v_lshlrev_b64 v[0:1], 12, v[12:13]
	v_lshl_add_u64 v[0:1], v[8:9], 0, v[0:1]
	s_waitcnt lgkmcnt(0)
	global_store_dwordx4 v[0:1], v[4:7], off sc1
	v_add_u32_e32 v0, 0x400, v14
	s_nop 0
	v_ashrrev_i32_e32 v4, 4, v0
	v_ashrrev_i32_e32 v5, 31, v4
	v_lshl_add_u32 v0, v4, 8, v15
	v_lshlrev_b64 v[4:5], 12, v[4:5]
	v_lshl_add_u64 v[10:11], v[8:9], 0, v[4:5]
	v_add_u32_e32 v4, 0x600, v14
	ds_read_b128 v[0:3], v0
	v_ashrrev_i32_e32 v12, 4, v4
	v_lshl_add_u32 v4, v12, 8, v15
	ds_read_b128 v[4:7], v4
	v_ashrrev_i32_e32 v13, 31, v12
	s_waitcnt lgkmcnt(1)
	global_store_dwordx4 v[10:11], v[0:3], off sc1
	s_nop 1
	v_lshlrev_b64 v[0:1], 12, v[12:13]
	v_lshl_add_u64 v[0:1], v[8:9], 0, v[0:1]
	s_waitcnt lgkmcnt(0)
	global_store_dwordx4 v[0:1], v[4:7], off sc1
	s_endpgm
